# serial round trips removed: barrier census, x1 un-sum LDS reads, PanelRms slots, small_from_hn weight staging
# speedup vs baseline: 1.0051x; 1.0051x over previous
; #define PG8_LAS __attribute__((address_space(3)))
; __device__ __forceinline__ void small_from_hn(const h16* __restrict__ hn, const h16* __restrict__ wsm16  , const float* __restrict__ fox_bf, const float* __restrict__ ml_bi, ...
;     ...
;     for (int q = 0; q < 4; ++q) { const int e = (q * NTHREADS + tid_) * 8, c = e >> 10, k = e & 1023;
;         *(PG8_LAS h16x8*)(L + (c * WP + k) * 2) = *(const h16x8*)(wsm16 + e); }
;     asm volatile("s_waitcnt vmcnt(0) lgkmcnt(0)" ::: "memory"); __syncthreads();
;     if (wave < 4) {
;         for (int blk = blockIdx.x; blk < TH / 64; blk += gridDim.x) {
;             const int R0 = blk * 64 + 16 * wave, i = lane & 15, gq = lane >> 4;
;             const h16* xr = hn + (size_t)(R0 + i) * DM + 8 * gq;
;             const PG8_LAS unsigned char* wr = L + (i * WP + 8 * gq) * 2;
; __global__ void __launch_bounds__(NTHREADS, 2) mega(MArgs a) {
;     ...
;             const h16* hnp = hf == 0 ? (const h16*)(ws + WS_HN) : (layer == 0 ? (const h16*)(a.out + (size_t)TH * DM) : (const h16*)(ws + WS_HN2));
;             small_from_hn(hnp, (const h16*)(ws + WS_WSM16) + layer * 16 * DM, a.in[3] + layer * 8, a.in[5] + layer * 4, a.in[6] + layer * 4, (float*)(ws + WS_SMALL), row0, L);
.LBB0_932:
	v_readlane_b32 s0, v255, 32
	s_cmp_eq_u32 s0, 1
	s_cbranch_scc0 .LBB0_1000
	v_readlane_b32 s0, v255, 31
	s_cmp_lt_u32 s0, 2
	v_readlane_b32 s0, v253, 54
	v_readlane_b32 s2, v253, 56
	v_readlane_b32 s1, v253, 55
	s_cselect_b32 s0, s0, s2
	v_readlane_b32 s2, v253, 57
	s_cselect_b32 s1, s1, s2
	v_readlane_b32 s2, v255, 42
	s_cmp_eq_u32 s2, 0
	v_readlane_b32 s2, v253, 24
	v_readlane_b32 s3, v253, 25
	s_cselect_b32 s3, s3, s1
	s_cselect_b32 s2, s2, s0
	v_readlane_b32 s0, v255, 36
	s_lshl_b32 s0, s0, 15
	v_readlane_b32 s4, v254, 2
	v_mov_b32_e32 v0, v243
	v_readlane_b32 s1, v255, 37
	v_readlane_b32 s5, v254, 3
	s_add_u32 s0, s4, s0
	s_addc_u32 s1, s5, 0
	v_lshlrev_b32_e32 v6, 3, v0
	v_ashrrev_i32_e32 v7, 31, v6
	v_lshl_add_u64 v[2:3], v[6:7], 1, s[0:1]
	global_load_dwordx4 v[2:5], v[2:3], off
	v_and_b32_e32 v1, 0x3f8, v6
	v_bfe_i32 v8, v0, 7, 22
	s_movk_i32 s4, 0x408
	v_mad_i32_i24 v7, v8, s4, v1
	v_lshl_add_u32 v7, v7, 1, 0
	v_add_u32_e32 v12, 0x1000, v6
	v_ashrrev_i32_e32 v13, 31, v12
	v_ashrrev_i32_e32 v9, 10, v12
	v_lshl_add_u64 v[12:13], v[12:13], 1, s[0:1]
	global_load_dwordx4 v[12:15], v[12:13], off
	v_mad_i32_i24 v9, v9, s4, v1
	v_lshl_add_u32 v9, v9, 1, 0
	v_add_u32_e32 v16, 0x2000, v6
	v_ashrrev_i32_e32 v17, 31, v16
	v_ashrrev_i32_e32 v10, 10, v16
	v_lshl_add_u64 v[16:17], v[16:17], 1, s[0:1]
	global_load_dwordx4 v[16:19], v[16:17], off
	v_mad_i32_i24 v10, v10, s4, v1
	v_lshl_add_u32 v10, v10, 1, 0
	v_add_u32_e32 v20, 0x3000, v6
	v_ashrrev_i32_e32 v21, 31, v20
	v_ashrrev_i32_e32 v6, 10, v20
	v_lshl_add_u64 v[20:21], v[20:21], 1, s[0:1]
	global_load_dwordx4 v[20:23], v[20:21], off
	v_mad_i32_i24 v1, v6, s4, v1
	v_lshl_add_u32 v1, v1, 1, 0
	v_readlane_b32 s0, v254, 63
	v_readlane_b32 s1, v255, 0
	s_waitcnt vmcnt(3)
	ds_write_b128 v7, v[2:5]
	s_waitcnt vmcnt(2)
	ds_write_b128 v9, v[12:15]
	s_waitcnt vmcnt(1)
	ds_write_b128 v10, v[16:19]
	s_waitcnt vmcnt(0)
	ds_write_b128 v1, v[20:23]
	v_ashrrev_i32_e32 v1, 6, v0
	s_waitcnt vmcnt(0) lgkmcnt(0)
	v_cmp_gt_i32_e32 vcc, 4, v1
	s_and_b64 s[0:1], vcc, s[0:1]
	s_waitcnt lgkmcnt(0)
	s_barrier
	s_and_saveexec_b64 s[14:15], s[0:1]
	s_cbranch_execz .LBB0_971
	v_readlane_b32 s0, v255, 36
	v_readlane_b32 s1, v255, 37
	s_lshl_b32 s28, s0, 2
	v_readlane_b32 s52, v253, 36
	s_mov_b32 s6, s0
	s_lshl_b64 s[0:1], s[28:29], 2
	v_readlane_b32 s64, v253, 48
	v_readlane_b32 s65, v253, 49
	s_add_u32 s4, s64, s0
	v_readlane_b32 s62, v253, 46
	s_addc_u32 s5, s65, s1
	v_lshlrev_b32_e32 v76, 4, v1
	v_and_b32_e32 v77, 15, v0
	v_bfe_u32 v1, v0, 4, 2
	v_readlane_b32 s63, v253, 47
	s_add_u32 s0, s62, s0
	v_lshlrev_b32_e32 v96, 4, v1
	v_mul_u32_u24_e32 v2, 0x408, v77
	s_addc_u32 s1, s63, s1
	s_lshl_b32 s28, s6, 3
	v_lshl_add_u64 v[68:69], s[2:3], 0, v[96:97]
	v_lshl_add_u32 v2, v1, 3, v2
	v_lshlrev_b32_e32 v96, 2, v77
	v_readlane_b32 s58, v253, 42
	s_lshl_b64 s[10:11], s[28:29], 2
	v_lshl_add_u32 v78, v2, 1, 0
	v_lshl_add_u64 v[2:3], s[4:5], 0, v[96:97]
	s_movk_i32 s4, 0xffd0
	v_lshl_add_u64 v[4:5], s[0:1], 0, v[96:97]
	s_movk_i32 s0, 0xffe0
	v_readlane_b32 s59, v253, 43
	s_add_u32 s10, s58, s10
	s_mov_b32 s5, -1
	s_mov_b32 s1, -1
	s_addc_u32 s11, s59, s11
	v_lshl_add_u64 v[2:3], v[2:3], 0, s[4:5]
	v_lshl_add_u64 v[4:5], v[4:5], 0, s[0:1]
	v_and_b32_e32 v0, 12, v0
	v_readlane_b32 s0, v255, 43
	v_cmp_gt_u32_e32 vcc, 12, v77
	v_lshl_add_u64 v[6:7], s[10:11], 0, v[96:97]
	v_cmp_ne_u32_e64 s[38:39], 8, v0
	v_lshl_or_b32 v79, v1, 2, s0
	v_cndmask_b32_e32 v0, v2, v4, vcc
	v_cndmask_b32_e32 v1, v3, v5, vcc
	v_cmp_gt_u32_e32 vcc, 8, v77
	v_lshl_add_u64 v[70:71], s[86:87], 0, v[96:97]
	v_readlane_b32 s4, v252, 0
	v_cndmask_b32_e32 v73, v1, v7, vcc
	v_cndmask_b32_e32 v72, v0, v6, vcc
	v_readlane_b32 s53, v253, 37
	v_readlane_b32 s54, v253, 38
	v_readlane_b32 s55, v253, 39
	v_readlane_b32 s56, v253, 40
	v_readlane_b32 s57, v253, 41
	v_readlane_b32 s60, v253, 44
	v_readlane_b32 s61, v253, 45
	v_readlane_b32 s66, v253, 50
	v_readlane_b32 s67, v253, 51
	s_branch .LBB0_946
